# group barriers (32 WGs of one batch element): skip L2 writeback / L1-only invalidate when every WG verifies at run time that XCC_ID == blockIdx%8 (flag in ctl area, checked after first grid barrier; o
# speedup vs baseline: 1.0441x; 1.0251x over previous
.LBB0_6:
	s_or_b64 exec, exec, s[2:3]
	s_mov_b32 s101, 0
	s_and_b32 s100, s89, 7
	s_cmp_eq_u32 s100, s33
	s_cbranch_scc1 .Lmy_xcc_ok
	s_mov_b64 s[4:5], exec
	s_mov_b64 exec, 1
	v_mov_b32_e32 v250, 0x3800
	v_mov_b32_e32 v251, 1
	global_atomic_add v250, v251, s[70:71]
	s_mov_b64 exec, s[4:5]
.Lmy_xcc_ok:
	s_lshr_b32 s90, s36, 6
	s_cmp_lt_i32 s78, 1
	s_cselect_b64 s[2:3], -1, 0
	s_cmp_gt_i32 s79, 0
	s_cselect_b64 s[4:5], -1, 0
	s_and_b64 s[2:3], s[2:3], s[4:5]
	s_and_b64 vcc, exec, s[2:3]
	s_cbranch_vccnz .LBB0_8
	s_add_u32 s2, s0, 0xd8
	s_addc_u32 s3, s1, 0
	v_writelane_b32 v252, s2, 2
	s_lshl_b32 s37, s90, 13
	s_nop 0
	v_writelane_b32 v252, s3, 3
	s_cbranch_execz .LBB0_9
	s_branch .LBB0_303

.LBB0_303:
	v_mov_b32_e32 v250, 0x3800
	global_load_dword v250, v250, s[70:71] sc1
	s_waitcnt vmcnt(0)
	v_readfirstlane_b32 s100, v250
	s_cmp_eq_u32 s100, 0
	s_cselect_b32 s101, 1, 0
	s_cmp_eq_u32 s78, 0
	s_cselect_b32 s101, s101, 0
	v_writelane_b32 v252, s68, 52
	s_add_i32 s0, s37, 0
	v_mov_b32_e32 v3, 0
	v_writelane_b32 v252, s69, 53
	v_writelane_b32 v252, s70, 54
	v_writelane_b32 v252, s71, 55
	v_writelane_b32 v252, s0, 56
	v_mov_b32_e32 v200, 1
	v_readlane_b32 s0, v252, 4
	v_readlane_b32 s8, v252, 12
	v_readlane_b32 s9, v252, 13
	s_add_u32 s0, s8, 0x400000
	v_readlane_b32 s1, v252, 5
	v_readlane_b32 s2, v252, 6
	v_readlane_b32 s3, v252, 7
	v_readlane_b32 s4, v252, 8
	v_readlane_b32 s5, v252, 9
	v_readlane_b32 s6, v252, 10
	v_readlane_b32 s7, v252, 11
	v_readlane_b32 s10, v252, 14
	v_readlane_b32 s11, v252, 15
	v_readlane_b32 s12, v252, 16
	v_readlane_b32 s13, v252, 17
	v_readlane_b32 s14, v252, 18
	v_readlane_b32 s15, v252, 19
	v_writelane_b32 v252, s0, 57
	s_addc_u32 s0, s9, 0
	v_writelane_b32 v252, s0, 58
	s_add_u32 s0, s10, 0x20000
	v_writelane_b32 v252, s0, 59
	s_addc_u32 s0, s11, 0
	v_writelane_b32 v252, s0, 60
	s_add_u32 s0, s14, 0x600000
	v_writelane_b32 v252, s0, 61
	s_addc_u32 s0, s15, 0
	v_writelane_b32 v252, s0, 62
	v_mov_b32_e32 v214, 0x3727c5ac
	v_readlane_b32 s8, v252, 20
	v_readlane_b32 s9, v252, 21
	s_add_u32 s0, s8, 0x400000
	s_addc_u32 s1, s9, 0
	v_readlane_b32 s10, v252, 22
	v_readlane_b32 s11, v252, 23
	v_readlane_b32 s12, v252, 24
	v_readlane_b32 s13, v252, 25
	v_readlane_b32 s14, v252, 26
	v_readlane_b32 s15, v252, 27
	v_readlane_b32 s16, v252, 28
	v_readlane_b32 s17, v252, 29
	v_readlane_b32 s18, v252, 30
	v_readlane_b32 s19, v252, 31
	v_readlane_b32 s20, v252, 32
	v_readlane_b32 s21, v252, 33
	v_readlane_b32 s22, v252, 34
	v_readlane_b32 s23, v252, 35
	v_writelane_b32 v252, s0, 63
	v_mov_b32_e32 v215, 0x260
	v_mov_b32_e32 v203, 0x8000
	v_writelane_b32 v253, s1, 0
	s_add_u32 s0, s14, 0x200000
	s_addc_u32 s1, s15, 0
	v_writelane_b32 v253, s0, 1
	v_mov_b32_e32 v202, 0x3e38aa3b
	v_mov_b32_e32 v216, 0xfffff400
	v_writelane_b32 v253, s1, 2
	s_add_u32 s0, s16, 0x400000
	s_addc_u32 s1, s17, 0
	v_writelane_b32 v253, s0, 3
	v_mov_b32_e32 v201, 0xfffffa00
	v_mov_b32_e32 v207, 0xff800000
	v_writelane_b32 v253, s1, 4
	s_add_u32 s0, s18, 0x200000
	s_addc_u32 s1, s19, 0
	v_writelane_b32 v253, s0, 5
	v_readlane_b32 s8, v252, 36
	v_readlane_b32 s9, v252, 37
	v_writelane_b32 v253, s1, 6
	s_add_u32 s0, s8, 0x100000
	s_addc_u32 s1, s9, 0
	v_readlane_b32 s16, v252, 44
	v_writelane_b32 v253, s0, 7
	v_readlane_b32 s17, v252, 45
	v_readlane_b32 s18, v252, 46
	v_writelane_b32 v253, s1, 8
	s_add_u32 s0, s16, 0x200000
	s_addc_u32 s1, s17, 0
	v_writelane_b32 v253, s0, 9
	v_readlane_b32 s19, v252, 47
	v_readlane_b32 s10, v252, 38
	v_writelane_b32 v253, s1, 10
	s_add_u32 s0, s18, 0x100000
	s_addc_u32 s1, s19, 0
	v_writelane_b32 v253, s0, 11
	v_readlane_b32 s11, v252, 39
	v_mov_b32_e32 v206, 0x80
	v_writelane_b32 v253, s1, 12
	s_add_u32 s0, s4, 0x1d18000
	s_addc_u32 s1, s5, 0
	v_writelane_b32 v253, s0, 13
	s_cmp_eq_u32 s33, 15
	v_mov_b32_e32 v219, 0x100
	v_writelane_b32 v253, s1, 14
	s_cselect_b64 s[0:1], -1, 0
	v_writelane_b32 v253, s0, 15
	s_cmp_eq_u32 s33, 14
	v_mov_b32_e32 v217, 0x200
	v_writelane_b32 v253, s1, 16
	s_cselect_b64 s[0:1], -1, 0
	v_writelane_b32 v253, s0, 17
	s_cmp_eq_u32 s33, 13
	v_mov_b32_e32 v218, 0x400
	v_writelane_b32 v253, s1, 18
	s_cselect_b64 s[0:1], -1, 0
	v_writelane_b32 v253, s0, 19
	s_cmp_eq_u32 s33, 12
	v_mov_b32_e32 v208, 0x800
	v_writelane_b32 v253, s1, 20
	s_cselect_b64 s[0:1], -1, 0
	v_writelane_b32 v253, s0, 21
	s_cmp_eq_u32 s33, 11
	v_mov_b32_e32 v209, 0x1000
	v_writelane_b32 v253, s1, 22
	s_cselect_b64 s[0:1], -1, 0
	v_writelane_b32 v253, s0, 23
	s_cmp_eq_u32 s33, 10
	v_mov_b32_e32 v210, 0x2000
	v_writelane_b32 v253, s1, 24
	s_cselect_b64 s[0:1], -1, 0
	v_writelane_b32 v253, s0, 25
	s_cmp_eq_u32 s33, 9
	v_mov_b32_e32 v211, 0x4000
	v_writelane_b32 v253, s1, 26
	s_cselect_b64 s[0:1], -1, 0
	v_writelane_b32 v253, s0, 27
	s_cmp_eq_u32 s33, 8
	v_mov_b32_e32 v212, 0x3f803f80
	v_writelane_b32 v253, s1, 28
	s_cselect_b64 s[0:1], -1, 0
	v_writelane_b32 v253, s0, 29
	s_cmp_eq_u32 s33, 7
	v_mov_b32_e32 v213, 0x3f80
	v_writelane_b32 v253, s1, 30
	s_cselect_b64 s[0:1], -1, 0
	v_writelane_b32 v253, s0, 31
	s_cmp_eq_u32 s33, 6
	s_mov_b32 s56, 1
	v_writelane_b32 v253, s1, 32
	s_cselect_b64 s[0:1], -1, 0
	v_writelane_b32 v253, s0, 33
	s_cmp_eq_u32 s33, 5
	s_movk_i32 s63, 0x100
	v_writelane_b32 v253, s1, 34
	s_cselect_b64 s[0:1], -1, 0
	v_writelane_b32 v253, s0, 35
	s_cmp_eq_u32 s33, 4
	s_movk_i32 s83, 0x2000
	v_writelane_b32 v253, s1, 36
	s_cselect_b64 s[0:1], -1, 0
	v_writelane_b32 v253, s0, 37
	s_cmp_eq_u32 s33, 3
	s_mov_b32 s82, 0x10000
	v_writelane_b32 v253, s1, 38
	s_cselect_b64 s[0:1], -1, 0
	v_writelane_b32 v253, s0, 39
	s_cmp_eq_u32 s33, 2
	s_movk_i32 s62, 0x4000
	v_writelane_b32 v253, s1, 40
	s_cselect_b64 s[0:1], -1, 0
	v_writelane_b32 v253, s0, 41
	s_cmp_eq_u32 s33, 1
	s_movk_i32 s77, 0x6000
	v_writelane_b32 v253, s1, 42
	s_cselect_b64 s[0:1], -1, 0
	v_writelane_b32 v253, s0, 43
	s_cmp_eq_u32 s33, 0
	s_mov_b32 s88, 0x8000
	v_writelane_b32 v253, s1, 44
	s_cselect_b64 s[0:1], -1, 0
	v_writelane_b32 v253, s0, 45
	s_add_i32 s2, 0, 0x10c00
	s_add_i32 s94, 0, 0x10400
	v_writelane_b32 v253, s1, 46
	s_lshl_b32 s0, s33, 6
	v_writelane_b32 v253, s0, 47
	s_lshl_b32 s0, s90, 7
	s_add_i32 s0, s0, 0
	s_mul_i32 s1, s90, 0x410
	s_add_i32 s0, s0, 0x21400
	s_add_i32 s91, s1, 0
	s_lshl_b32 s1, s90, 12
	v_writelane_b32 v253, s0, 48
	s_lshl_b32 s0, s90, 8
	s_add_i32 s1, s2, s1
	s_add_i32 s33, s0, 0
	v_writelane_b32 v253, s1, 49
	s_add_i32 s96, s94, s0
	s_lshl_b32 s0, s90, 4
	s_add_i32 s1, s90, 8
	v_writelane_b32 v253, s2, 50
	s_and_b32 s71, s0, 48
	s_sub_i32 s81, s91, s0
	s_lshl_b32 s0, s1, 3
	s_lshl_b32 s1, s1, 10
	v_writelane_b32 v253, s1, 51
	s_mul_i32 s1, s90, 0x3f0
	s_add_i32 s7, s91, s1
	s_sub_i32 s1, s90, 64
	s_add_i32 s70, s2, s37
	v_writelane_b32 v253, s1, 52
	s_lshl_b32 s92, s90, 5
	s_lshl_b32 s3, s90, 3
	s_lshl_b32 s8, s90, 10
	s_lshr_b32 s2, s36, 7
	s_add_i32 s33, s33, 0x20400
	s_and_b32 s1, s3, 0x1fffffe0
	s_add_i32 s97, s94, s8
	v_writelane_b32 v253, s2, 53
	s_and_b32 s93, s92, 32
	s_and_b32 s2, s0, 0x3fffffe0
	s_cmp_gt_u32 s36, 63
	s_cselect_b64 s[4:5], -1, 0
	v_writelane_b32 v253, s4, 54
	s_mov_b32 s72, 0xa000
	s_mov_b32 s66, 0xc000
	v_writelane_b32 v253, s5, 55
	s_add_i32 s4, s90, -4
	s_lshr_b32 s5, s4, 2
	s_add_i32 s5, s5, 1
	s_cmpk_gt_u32 s36, 0xff
	s_cselect_b64 s[10:11], -1, 0
	s_and_b32 s9, s90, 0x3fffffc
	s_and_b32 s6, s5, 7
	v_writelane_b32 v253, s10, 56
	s_cmp_gt_u32 s4, 27
	s_movk_i32 s16, 0xc00
	v_writelane_b32 v253, s11, 57
	s_cselect_b64 s[10:11], -1, 0
	v_writelane_b32 v253, s10, 58
	s_and_b32 s4, s5, 0x7ffffff8
	s_cmp_lg_u32 s6, 0
	v_writelane_b32 v253, s11, 59
	v_writelane_b32 v253, s4, 60
	s_cselect_b64 s[4:5], -1, 0
	v_writelane_b32 v253, s4, 61
	s_cmp_lg_u32 s90, s9
	s_mov_b32 s11, 0
	v_writelane_b32 v253, s5, 62
	s_cselect_b64 s[4:5], -1, 0
	v_writelane_b32 v254, s4, 0
	v_writelane_b32 v253, s9, 63
	s_movk_i32 s57, 0x300
	v_writelane_b32 v254, s5, 1
	v_writelane_b32 v254, s8, 2
	s_add_i32 s5, s8, 0
	s_lshr_b32 s4, s36, 2
	v_writelane_b32 v254, s5, 3
	s_add_i32 s5, s5, 0x8400
	v_writelane_b32 v254, s5, 4
	s_and_b32 s5, s4, 0x3fffffc0
	s_add_u32 s5, s5, 0x5d088000
	v_writelane_b32 v254, s5, 5
	s_addc_u32 s5, 0, 0
	s_and_b32 s4, s4, 0x3ffffff0
	v_writelane_b32 v254, s5, 6
	s_add_u32 s4, s4, 0x5d088000
	v_writelane_b32 v254, s4, 7
	s_addc_u32 s4, 0, 0
	v_writelane_b32 v254, s4, 8
	s_lshl_b32 s10, s3, 1
	s_lshl_b32 s3, s6, 4
	v_writelane_b32 v254, s3, 9
	s_mul_i32 s3, s90, 0xfffff804
	v_writelane_b32 v254, s7, 10
	s_add_i32 s3, s7, s3
	v_writelane_b32 v254, s3, 11
	s_add_i32 s3, 0, 0x21160
	v_writelane_b32 v254, s3, 12
	s_add_i32 s3, 0, 0x21164
	v_writelane_b32 v254, s3, 13
	s_add_i32 s3, 0, 0x22800
	v_writelane_b32 v254, s3, 14
	s_add_i32 s3, 0, 0x22000
	v_writelane_b32 v254, s3, 15
	s_add_i32 s3, 0, 0x21800
	v_writelane_b32 v254, s3, 16
	s_add_i32 s3, 0, 0x21d04
	v_writelane_b32 v254, s3, 17
	s_add_i32 s3, 0, 0x21c04
	v_writelane_b32 v254, s3, 18
	s_add_i32 s3, 0, 0x21c08
	v_writelane_b32 v254, s3, 19
	s_add_i32 s3, 0, 0x21c0c
	v_writelane_b32 v254, s3, 20
	s_add_i32 s3, 0, 0x21c10
	v_writelane_b32 v254, s3, 21
	s_add_i32 s3, 0, 0x21c14
	v_writelane_b32 v254, s3, 22
	s_add_i32 s3, s91, 0x2080
	v_writelane_b32 v254, s3, 23
	s_add_i32 s3, s91, 0x4100
	v_writelane_b32 v254, s3, 24
	s_add_i32 s3, s91, 0x6180
	v_writelane_b32 v254, s3, 25
	s_add_i32 s3, 0, 0x21c1c
	v_writelane_b32 v254, s3, 26
	s_add_i32 s3, 0, 0x21600
	v_writelane_b32 v254, s3, 27
	s_add_i32 s3, 0, 0x21604
	v_writelane_b32 v254, s3, 28
	s_add_i32 s3, s81, 0xa400
	v_writelane_b32 v254, s3, 29
	s_add_i32 s3, s91, 0x8200
	v_writelane_b32 v254, s3, 30
	s_add_i32 s3, 0, 0x18400
	v_writelane_b32 v254, s3, 31
	s_add_i32 s3, s91, 0xa280
	v_writelane_b32 v254, s3, 32
	s_add_i32 s3, s91, 0xc300
	v_writelane_b32 v254, s3, 33
	s_add_i32 s3, 0, 0x1c400
	v_writelane_b32 v254, s3, 34
	s_add_i32 s3, s91, 0xe380
	v_writelane_b32 v254, s3, 35
	s_lshl_b32 s4, s1, 1
	v_writelane_b32 v254, s4, 36
	s_lshl_b32 s0, s0, 1
	s_movk_i32 s17, 0x7fff
	v_writelane_b32 v254, s5, 37
	v_writelane_b32 v254, s0, 38
	s_mov_b32 s18, 0xff800000
	s_mov_b32 s19, 0x10001
	v_writelane_b32 v254, s1, 39
	s_lshl_b32 s0, s2, 1
	v_writelane_b32 v254, s0, 40
	s_mov_b32 s2, s11
	s_movk_i32 s67, 0xe3f
	v_writelane_b32 v254, s1, 41
	s_add_i32 s0, 0, 0x820
	v_writelane_b32 v254, s0, 42
	v_writelane_b32 v254, s2, 43
	s_mov_b64 s[0:1], 0
	s_mov_b64 s[50:51], -1
	v_writelane_b32 v254, s3, 44
	v_writelane_b32 v254, s89, 45
	v_writelane_b32 v254, s78, 46
	s_mov_b64 s[24:25], 0x80
	s_mov_b64 s[26:27], 0x2000
	v_writelane_b32 v254, s79, 47
	v_writelane_b32 v254, s95, 48
	v_writelane_b32 v254, s90, 49
	v_writelane_b32 v254, s94, 50
	v_writelane_b32 v254, s70, 51
	v_writelane_b32 v254, s71, 52
	v_writelane_b32 v254, s92, 53
	s_mov_b64 s[64:65], 0x800
	s_mov_b32 s80, 0x3e0293ee
	s_mov_b32 s84, 0x3f803f80
	v_writelane_b32 v254, s93, 54
	v_readlane_b32 s12, v252, 40
	v_readlane_b32 s13, v252, 41
	v_readlane_b32 s14, v252, 42
	v_readlane_b32 s15, v252, 43
	v_readlane_b32 s20, v252, 48
	v_readlane_b32 s21, v252, 49
	v_readlane_b32 s22, v252, 50
	v_readlane_b32 s23, v252, 51
	s_branch .LBB0_307
.LBB0_304:
	s_or_b64 exec, exec, s[4:5]
	s_waitcnt vmcnt(0)
	s_cmp_lg_u32 s101, 0
	s_cbranch_scc1 .Lmy_gi_11
	buffer_inv sc1
.Lmy_gi_11:
	buffer_inv sc0
	s_waitcnt vmcnt(0)

.LBB0_1148:
	s_and_b64 vcc, exec, s[0:1]
	s_cbranch_vccz .LBB0_1166
	v_readlane_b32 s0, v252, 52
	v_readlane_b32 s2, v252, 54
	v_readlane_b32 s3, v252, 55
	s_mov_b64 s[6:7], s[2:3]
	v_mbcnt_lo_u32_b32 v0, -1, 0
	v_mbcnt_hi_u32_b32 v0, -1, v0
	s_waitcnt vmcnt(0)
	v_readlane_b32 s1, v252, 53
	v_or_b32_e32 v0, s95, v0
	v_cmp_eq_u32_e32 vcc, 0, v0
	s_waitcnt vmcnt(0) lgkmcnt(0)
	s_barrier
	s_and_saveexec_b64 s[0:1], vcc
	s_cbranch_execz .LBB0_1165
	s_lshl_b32 s2, s30, 7
	s_and_b32 s2, s2, 0x380
	s_mov_b64 s[4:5], exec
	s_add_u32 s2, s6, s2
	s_addc_u32 s3, s7, 0
	s_cmp_lg_u32 s101, 0
	s_cbranch_scc1 .Lmy_gw_0
	buffer_wbl2 sc1
.Lmy_gw_0:
	s_waitcnt vmcnt(0)
	v_mbcnt_lo_u32_b32 v0, s4, 0
	s_add_u32 s2, s2, 0x18000
	v_mbcnt_hi_u32_b32 v0, s5, v0
	s_addc_u32 s3, s3, 0
	v_cmp_eq_u32_e32 vcc, 0, v0
	s_and_saveexec_b64 s[8:9], vcc
	s_cbranch_execz .LBB0_1152
	s_bcnt1_i32_b64 s4, s[4:5]
	v_mov_b32_e32 v1, s4
	global_atomic_add v1, v3, v1, s[2:3] sc0

.LBB0_1231:
	s_waitcnt vmcnt(0)
	s_waitcnt vmcnt(0) lgkmcnt(0)
	buffer_inv sc0
	s_waitcnt vmcnt(0)
	s_barrier
	v_mbcnt_lo_u32_b32 v0, -1, 0
	v_mbcnt_hi_u32_b32 v0, -1, v0
	s_movk_i32 s6, 0x100
	v_or_b32_e32 v2, s95, v0
	s_andn2_b64 vcc, exec, s[54:55]
	v_readfirstlane_b32 s8, v2
	s_cbranch_vccnz .LBB0_1251
	v_lshlrev_b32_e32 v1, 4, v2
	v_add_u32_e32 v0, 0x2000, v1
	v_ashrrev_i32_e32 v4, 31, v0
	v_lshrrev_b32_e32 v4, 22, v4
	v_add_u32_e32 v4, v0, v4
	v_ashrrev_i32_e32 v16, 10, v4
	v_mul_i32_i24_e32 v4, 0x400, v16
	v_sub_u32_e32 v0, v0, v4
	v_lshrrev_b32_e32 v4, 4, v0
	v_bitop3_b32 v0, v4, v0, 32 bitop3:0x6c
	v_ashrrev_i32_e32 v4, 31, v0
	v_lshrrev_b32_e32 v4, 26, v4
	v_add_u32_e32 v4, v0, v4
	v_lshlrev_b32_e32 v5, 3, v16
	v_ashrrev_i32_e32 v17, 6, v4
	v_and_b32_e32 v5, -16, v5
	v_add_u32_e32 v5, v17, v5
	v_and_b32_e32 v6, 3, v17
	s_mov_b32 s13, 0x7fffffe0
	v_lshrrev_b32_e32 v7, 2, v5
	v_lshlrev_b32_e32 v8, 1, v5
	v_and_b32_e32 v4, 0xc0, v4
	v_and_or_b32 v6, v5, s13, v6
	v_and_b32_e32 v7, 4, v7
	v_and_b32_e32 v8, 24, v8
	v_sub_u32_e32 v0, v0, v4
	v_or3_b32 v6, v6, v7, v8
	v_lshlrev_b32_e32 v7, 5, v16
	v_ashrrev_i16_sdwa v0, v200, sext(v0) dst_sel:DWORD dst_unused:UNUSED_PAD src0_sel:DWORD src1_sel:BYTE_0
	v_and_b32_e32 v7, 32, v7
	v_bfe_i32 v18, v0, 0, 16
	v_mul_lo_u32 v6, v6, s6
	v_add_u32_e32 v4, v7, v18
	v_lshlrev_b32_e32 v5, 9, v5
	v_add_lshl_u32 v0, v6, v4, 1
	v_lshl_add_u32 v68, v4, 1, v5
	v_bfe_i32 v4, v2, 27, 1
	v_lshrrev_b32_e32 v4, 22, v4
	v_add_u32_e32 v4, v1, v4
	v_and_b32_e32 v4, 0xfffffc00, v4
	v_sub_u32_e32 v1, v1, v4
	v_lshrrev_b32_e32 v4, 4, v1
	v_ashrrev_i32_e32 v5, 31, v2
	v_bitop3_b32 v1, v4, v1, 32 bitop3:0x6c
	v_lshrrev_b32_e32 v5, 26, v5
	s_ashr_i32 s12, s8, 6
	s_ashr_i32 s7, s6, 31
	v_ashrrev_i32_e32 v4, 31, v1
	v_add_u32_e32 v5, v2, v5
	s_ashr_i32 s9, s8, 8
	s_lshl_b64 s[0:1], s[6:7], 8
	s_lshl_b64 s[2:3], s[6:7], 9
	s_lshl_b32 s30, s12, 10
	v_lshrrev_b32_e32 v4, 26, v4
	v_ashrrev_i32_e32 v20, 6, v5
	s_add_u32 s41, s50, 0x1100000
	v_add_u32_e32 v4, v1, v4
	v_lshlrev_b32_e32 v5, 3, v20
	s_addc_u32 s54, s51, 0
	s_lshl_b64 s[4:5], s[46:47], 17
	v_ashrrev_i32_e32 v19, 6, v4
	v_and_b32_e32 v5, -16, v5
	s_add_u32 s50, s48, s4
	v_add_u32_e32 v5, v19, v5
	s_addc_u32 s51, s49, s5
	v_and_b32_e32 v6, 3, v19
	v_lshrrev_b32_e32 v7, 2, v5
	v_lshlrev_b32_e32 v8, 1, v5
	v_and_b32_e32 v4, 0xc0, v4
	s_add_u32 s4, s50, 0x10000
	v_and_or_b32 v6, v5, s13, v6
	v_and_b32_e32 v7, 4, v7
	v_and_b32_e32 v8, 24, v8
	v_sub_u32_e32 v1, v1, v4
	s_addc_u32 s5, s51, 0
	v_or3_b32 v6, v6, v7, v8
	v_lshlrev_b32_e32 v7, 5, v20
	v_ashrrev_i16_sdwa v1, v200, sext(v1) dst_sel:DWORD dst_unused:UNUSED_PAD src0_sel:DWORD src1_sel:BYTE_0
	s_lshr_b64 s[20:21], s[6:7], 23
	s_mul_i32 s14, s2, s22
	v_and_b32_e32 v7, 32, v7
	v_bfe_i32 v21, v1, 0, 16
	s_mul_i32 s13, s20, s22
	s_add_u32 s52, s41, s14
	v_mul_lo_u32 v6, v6, s6
	v_add_u32_e32 v1, v7, v21
	s_addc_u32 s53, s54, s13
	s_add_i32 s47, s30, 0
	v_add_lshl_u32 v70, v6, v1, 1
	s_add_i32 m0, s47, 0x10000
	v_lshlrev_b32_e32 v4, 9, v5
	global_load_lds_dwordx4 v70, s[52:53]
	s_add_i32 m0, s47, 0x12000
	s_add_u32 s20, s52, s0
	s_addc_u32 s21, s53, s1
	s_add_i32 s55, s47, 0x14000
	global_load_lds_dwordx4 v0, s[52:53]
	s_mov_b32 m0, s55
	s_add_i32 s56, s47, 0x16000
	global_load_lds_dwordx4 v70, s[20:21]
	s_mov_b32 m0, s56
	v_lshl_add_u32 v72, v1, 1, v4
	global_load_lds_dwordx4 v0, s[20:21]
	s_mov_b32 m0, s47
	s_add_i32 s57, s47, 0x2000
	global_load_lds_dwordx4 v72, s[50:51]
	s_mov_b32 m0, s57
	s_add_i32 s58, s47, 0x4000
	global_load_lds_dwordx4 v68, s[50:51]
	s_mov_b32 m0, s58
	s_add_i32 s59, s47, 0x6000
	global_load_lds_dwordx4 v72, s[4:5]
	s_mov_b32 m0, s59
	v_mov_b32_e32 v71, v3
	global_load_lds_dwordx4 v68, s[4:5]
	v_mov_b32_e32 v1, v3
	v_mov_b32_e32 v73, v3
	v_mov_b32_e32 v69, v3
	s_cmp_eq_u32 s9, 1
	s_movk_i32 s85, 0x4000
	v_lshl_add_u64 v[4:5], s[52:53], 0, v[70:71]
	v_lshl_add_u64 v[6:7], s[52:53], 0, v[0:1]
	v_lshl_add_u64 v[8:9], s[20:21], 0, v[70:71]
	v_lshl_add_u64 v[10:11], s[20:21], 0, v[0:1]
	v_lshl_add_u64 v[12:13], s[50:51], 0, v[72:73]
	v_lshl_add_u64 v[14:15], s[50:51], 0, v[68:69]
	s_cselect_b64 s[4:5], -1, 0
	s_cmp_lg_u32 s9, 1
	s_cbranch_scc1 .LBB0_1234
	s_barrier

.LBB0_1314:
	s_and_b64 vcc, exec, s[0:1]
	s_cbranch_vccz .LBB0_1332
	v_readlane_b32 s0, v252, 52
	v_readlane_b32 s2, v252, 54
	v_readlane_b32 s3, v252, 55
	s_mov_b64 s[6:7], s[2:3]
	v_mbcnt_lo_u32_b32 v0, -1, 0
	v_mbcnt_hi_u32_b32 v0, -1, v0
	s_waitcnt vmcnt(0)
	v_readlane_b32 s1, v252, 53
	v_or_b32_e32 v0, s95, v0
	v_cmp_eq_u32_e32 vcc, 0, v0
	s_waitcnt vmcnt(0) lgkmcnt(0)
	s_barrier
	s_and_saveexec_b64 s[0:1], vcc
	s_cbranch_execz .LBB0_1331
	s_lshl_b32 s2, s31, 7
	s_and_b32 s2, s2, 0x380
	s_mov_b64 s[4:5], exec
	s_add_u32 s2, s6, s2
	s_addc_u32 s3, s7, 0
	s_cmp_lg_u32 s101, 0
	s_cbranch_scc1 .Lmy_gw_1
	buffer_wbl2 sc1

.LBB0_2003:
	s_and_b64 vcc, exec, s[0:1]
	s_cbranch_vccz .LBB0_2021
	v_readlane_b32 s0, v252, 52
	v_readlane_b32 s2, v252, 54
	v_readlane_b32 s3, v252, 55
	s_mov_b64 s[6:7], s[2:3]
	v_mbcnt_lo_u32_b32 v0, -1, 0
	v_mbcnt_hi_u32_b32 v0, -1, v0
	s_waitcnt vmcnt(0)
	v_readlane_b32 s1, v252, 53
	v_or_b32_e32 v0, s95, v0
	v_cmp_eq_u32_e32 vcc, 0, v0
	s_barrier
	s_and_saveexec_b64 s[0:1], vcc
	s_cbranch_execz .LBB0_2020
	s_lshl_b32 s2, s30, 7
	s_and_b32 s2, s2, 0x380
	s_mov_b64 s[4:5], exec
	s_add_u32 s2, s6, s2
	s_addc_u32 s3, s7, 0
	s_cmp_lg_u32 s101, 0
	s_cbranch_scc1 .Lmy_gw_2
	buffer_wbl2 sc1
.Lmy_gw_2:
	s_waitcnt vmcnt(0)
	s_waitcnt vmcnt(0)
	v_mbcnt_lo_u32_b32 v0, s4, 0
	s_add_u32 s2, s2, 0x18000
	v_mbcnt_hi_u32_b32 v0, s5, v0
	s_addc_u32 s3, s3, 0
	v_cmp_eq_u32_e32 vcc, 0, v0
	s_and_saveexec_b64 s[8:9], vcc
	s_cbranch_execz .LBB0_2007
	s_bcnt1_i32_b64 s4, s[4:5]
	v_mov_b32_e32 v1, s4
	global_atomic_add v1, v3, v1, s[2:3] sc0

.LBB0_2104:
	s_and_b64 vcc, exec, s[0:1]
	s_cbranch_vccz .LBB0_2122
	v_readlane_b32 s0, v252, 52
	v_readlane_b32 s2, v252, 54
	v_readlane_b32 s3, v252, 55
	s_mov_b64 s[6:7], s[2:3]
	v_mbcnt_lo_u32_b32 v0, -1, 0
	v_mbcnt_hi_u32_b32 v0, -1, v0
	s_waitcnt vmcnt(0)
	v_readlane_b32 s1, v252, 53
	v_or_b32_e32 v0, s95, v0
	v_cmp_eq_u32_e32 vcc, 0, v0
	s_waitcnt vmcnt(0)
	s_barrier
	s_and_saveexec_b64 s[0:1], vcc
	s_cbranch_execz .LBB0_2121
	s_lshl_b32 s2, s30, 7
	s_and_b32 s2, s2, 0x380
	s_mov_b64 s[4:5], exec
	s_add_u32 s2, s6, s2
	s_addc_u32 s3, s7, 0
	s_cmp_lg_u32 s101, 0
	s_cbranch_scc1 .Lmy_gw_3
	buffer_wbl2 sc1

.LBB0_3263:
	s_lshl_b32 s2, s30, 7
	s_and_b32 s2, s2, 0x380
	s_mov_b64 s[4:5], exec
	s_add_u32 s2, s6, s2
	s_addc_u32 s3, s7, 0
	s_cmp_lg_u32 s101, 0
	s_cbranch_scc1 .Lmy_gw_11
	buffer_wbl2 sc1

	.amdhsa_kernel _Z6mk_fwd4Args
		.amdhsa_group_segment_fixed_size 0
		.amdhsa_private_segment_fixed_size 0
		.amdhsa_kernarg_size 472
		.amdhsa_user_sgpr_count 2
		.amdhsa_user_sgpr_dispatch_ptr 0
		.amdhsa_user_sgpr_queue_ptr 0
		.amdhsa_user_sgpr_kernarg_segment_ptr 1
		.amdhsa_user_sgpr_dispatch_id 0
		.amdhsa_user_sgpr_kernarg_preload_length 0
		.amdhsa_user_sgpr_kernarg_preload_offset 0
		.amdhsa_user_sgpr_private_segment_size 0
		.amdhsa_uses_dynamic_stack 0
		.amdhsa_enable_private_segment 0
		.amdhsa_system_sgpr_workgroup_id_x 1
		.amdhsa_system_sgpr_workgroup_id_y 0
		.amdhsa_system_sgpr_workgroup_id_z 0
		.amdhsa_system_sgpr_workgroup_info 0
		.amdhsa_system_vgpr_workitem_id 0
		.amdhsa_next_free_vgpr 256
		.amdhsa_next_free_sgpr 102
		.amdhsa_accum_offset 256
		.amdhsa_reserve_vcc 1
		.amdhsa_float_round_mode_32 0
		.amdhsa_float_round_mode_16_64 0
		.amdhsa_float_denorm_mode_32 3
		.amdhsa_float_denorm_mode_16_64 3
		.amdhsa_dx10_clamp 1
		.amdhsa_ieee_mode 1
		.amdhsa_fp16_overflow 0
		.amdhsa_tg_split 0
		.amdhsa_exception_fp_ieee_invalid_op 0
		.amdhsa_exception_fp_denorm_src 0
		.amdhsa_exception_fp_ieee_div_zero 0
		.amdhsa_exception_fp_ieee_overflow 0
		.amdhsa_exception_fp_ieee_underflow 0
		.amdhsa_exception_fp_ieee_inexact 0
		.amdhsa_exception_int_div_zero 0
	.end_amdhsa_kernel

amdhsa.kernels:
  - .agpr_count:     0
    .args:
      - .offset:         0
        .size:           216
        .value_kind:     by_value
      - .offset:         216
        .size:           4
        .value_kind:     hidden_block_count_x
      - .offset:         220
        .size:           4
        .value_kind:     hidden_block_count_y
      - .offset:         224
        .size:           4
        .value_kind:     hidden_block_count_z
      - .offset:         228
        .size:           2
        .value_kind:     hidden_group_size_x
      - .offset:         230
        .size:           2
        .value_kind:     hidden_group_size_y
      - .offset:         232
        .size:           2
        .value_kind:     hidden_group_size_z
      - .offset:         234
        .size:           2
        .value_kind:     hidden_remainder_x
      - .offset:         236
        .size:           2
        .value_kind:     hidden_remainder_y
      - .offset:         238
        .size:           2
        .value_kind:     hidden_remainder_z
      - .offset:         256
        .size:           8
        .value_kind:     hidden_global_offset_x
      - .offset:         264
        .size:           8
        .value_kind:     hidden_global_offset_y
      - .offset:         272
        .size:           8
        .value_kind:     hidden_global_offset_z
      - .offset:         280
        .size:           2
        .value_kind:     hidden_grid_dims
      - .offset:         336
        .size:           4
        .value_kind:     hidden_dynamic_lds_size
    .group_segment_fixed_size: 0
    .kernarg_segment_align: 8
    .kernarg_segment_size: 472
    .language:       OpenCL C
    .language_version:
      - 2
      - 0
    .max_flat_workgroup_size: 512
    .name:           _Z6mk_fwd4Args
    .private_segment_fixed_size: 0
    .sgpr_count:     108
    .sgpr_spill_count: 258
    .symbol:         _Z6mk_fwd4Args.kd
    .uniform_work_group_size: 1
    .uses_dynamic_stack: false
    .vgpr_count:     256
    .vgpr_spill_count: 0
    .wavefront_size: 64
